# GEMM1 epilogue: hoist all 16 rot loads before the store groups, drop per-group vmcnt waits
# baseline (speedup 1.0000x reference)
.LBB0_230:
	v_lshl_or_b32 v154, s28, 8, v158
	s_and_b32 s2, s28, -4
	s_cmp_eq_u32 s2, 20
	v_and_b32_e32 v130, 56, v154
	v_lshl_add_u32 v162, s30, 8, v156
	s_cselect_b64 s[30:31], -1, 0
	v_cmp_gt_u32_e32 vcc, 16, v130
	s_and_b64 s[30:31], s[30:31], vcc
	s_cmp_lt_i32 s28, 4
	s_cselect_b64 s[28:29], -1, 0
	s_and_b64 s[34:35], s[28:29], exec
	s_cselect_b32 s2, 0, 32
	v_lshrrev_b32_e32 v130, 1, v130
	s_or_b64 s[28:29], s[28:29], s[30:31]
	v_or_b32_e32 v148, s2, v130
	v_mov_b32_e32 v131, 0
	v_mov_b32_e32 v130, 1.0
	v_mov_b32_e32 v136, 1.0
	v_mov_b32_e32 v137, 0
	v_mov_b32_e32 v138, 1.0
	v_mov_b32_e32 v139, 0
	v_mov_b32_e32 v132, 1.0
	v_mov_b32_e32 v133, 0
	v_mov_b32_e32 v134, 1.0
	v_mov_b32_e32 v135, 0
	s_and_saveexec_b64 s[30:31], s[28:29]
	s_cbranch_execz .Lg1pre_skip_L0
	v_mad_i64_i32 v[238:239], s[34:35], v162, 40, v[148:149]
	v_lshl_add_u64 v[238:239], v[238:239], 3, s[12:13]
	global_load_dwordx4 v[170:173], v[238:239], off
	global_load_dwordx4 v[174:177], v[238:239], off offset:16
	v_add_u32_e32 v238, 0x10, v162
	v_mad_i64_i32 v[238:239], s[34:35], v238, 40, v[148:149]
	v_lshl_add_u64 v[238:239], v[238:239], 3, s[12:13]
	global_load_dwordx4 v[178:181], v[238:239], off
	global_load_dwordx4 v[182:185], v[238:239], off offset:16
	v_add_u32_e32 v238, 0x20, v162
	v_mad_i64_i32 v[238:239], s[34:35], v238, 40, v[148:149]
	v_lshl_add_u64 v[238:239], v[238:239], 3, s[12:13]
	global_load_dwordx4 v[186:189], v[238:239], off
	global_load_dwordx4 v[190:193], v[238:239], off offset:16
	v_add_u32_e32 v238, 0x30, v162
	v_mad_i64_i32 v[238:239], s[34:35], v238, 40, v[148:149]
	v_lshl_add_u64 v[238:239], v[238:239], 3, s[12:13]
	global_load_dwordx4 v[194:197], v[238:239], off
	global_load_dwordx4 v[198:201], v[238:239], off offset:16
	v_add_u32_e32 v238, 0x80, v162
	v_mad_i64_i32 v[238:239], s[34:35], v238, 40, v[148:149]
	v_lshl_add_u64 v[238:239], v[238:239], 3, s[12:13]
	global_load_dwordx4 v[202:205], v[238:239], off
	global_load_dwordx4 v[206:209], v[238:239], off offset:16
	v_add_u32_e32 v238, 0x90, v162
	v_mad_i64_i32 v[238:239], s[34:35], v238, 40, v[148:149]
	v_lshl_add_u64 v[238:239], v[238:239], 3, s[12:13]
	global_load_dwordx4 v[210:213], v[238:239], off
	global_load_dwordx4 v[214:217], v[238:239], off offset:16
	v_add_u32_e32 v238, 0xa0, v162
	v_mad_i64_i32 v[238:239], s[34:35], v238, 40, v[148:149]
	v_lshl_add_u64 v[238:239], v[238:239], 3, s[12:13]
	global_load_dwordx4 v[218:221], v[238:239], off
	global_load_dwordx4 v[222:225], v[238:239], off offset:16
	v_add_u32_e32 v238, 0xb0, v162
	v_mad_i64_i32 v[238:239], s[34:35], v238, 40, v[148:149]
	v_lshl_add_u64 v[238:239], v[238:239], 3, s[12:13]
	global_load_dwordx4 v[226:229], v[238:239], off
	global_load_dwordx4 v[234:237], v[238:239], off offset:16
.Lg1pre_skip_L0:
	s_or_b64 exec, exec, s[30:31]
	s_waitcnt vmcnt(0)
	s_and_saveexec_b64 s[30:31], s[28:29]
	s_cbranch_execz .LBB0_232
	v_mad_i64_i32 v[132:133], s[34:35], v162, 40, v[148:149]
	v_lshl_add_u64 v[132:133], v[132:133], 3, s[12:13]
	v_mov_b64_e32 v[136:137], v[170:171]
	v_mov_b64_e32 v[138:139], v[172:173]
	s_nop 0
	v_mov_b64_e32 v[132:133], v[174:175]
	v_mov_b64_e32 v[134:135], v[176:177]
.LBB0_232:
	s_or_b64 exec, exec, s[30:31]
	s_waitcnt vmcnt(0)
	v_pk_mul_f32 v[166:167], v[128:129], v[138:139]
	v_pk_mul_f32 v[168:169], v[126:127], v[136:137]
	v_pk_mul_f32 v[126:127], v[126:127], v[136:137] op_sel:[1,0] op_sel_hi:[0,1]
	v_pk_mul_f32 v[128:129], v[128:129], v[138:139] op_sel:[1,0] op_sel_hi:[0,1]
	v_add_f32_e32 v126, v126, v127
	v_sub_f32_e32 v127, v166, v167
	v_add_f32_e32 v128, v128, v129
	v_sub_f32_e32 v163, v168, v169
	v_cvt_pk_bf16_f32 v126, v163, v126
	v_cvt_pk_bf16_f32 v127, v127, v128
	v_pk_mul_f32 v[128:129], v[122:123], v[132:133]
	v_pk_mul_f32 v[122:123], v[122:123], v[132:133] op_sel:[1,0] op_sel_hi:[0,1]
	v_sub_f32_e32 v128, v128, v129
	v_add_f32_e32 v122, v122, v123
	v_pk_mul_f32 v[166:167], v[124:125], v[134:135]
	v_cvt_pk_bf16_f32 v128, v128, v122
	v_pk_mul_f32 v[122:123], v[124:125], v[134:135] op_sel:[1,0] op_sel_hi:[0,1]
	v_mov_b64_e32 v[164:165], s[10:11]
	v_sub_f32_e32 v129, v166, v167
	v_add_f32_e32 v122, v122, v123
	v_ashrrev_i32_e32 v155, 31, v154
	v_mad_i64_i32 v[164:165], s[30:31], v162, s53, v[164:165]
	v_cvt_pk_bf16_f32 v129, v129, v122
	v_pk_mul_f32 v[122:123], v[120:121], v[138:139]
	v_pk_mul_f32 v[124:125], v[118:119], v[136:137]
	v_pk_mul_f32 v[118:119], v[118:119], v[136:137] op_sel:[1,0] op_sel_hi:[0,1]
	v_pk_mul_f32 v[120:121], v[120:121], v[138:139] op_sel:[1,0] op_sel_hi:[0,1]
	v_lshl_add_u64 v[164:165], v[154:155], 1, v[164:165]
	v_add_f32_e32 v118, v118, v119
	v_sub_f32_e32 v119, v122, v123
	v_add_f32_e32 v120, v120, v121
	global_store_dwordx4 v[164:165], v[126:129], off nt
	v_sub_f32_e32 v124, v124, v125
	v_cvt_pk_bf16_f32 v118, v124, v118
	v_cvt_pk_bf16_f32 v119, v119, v120
	v_pk_mul_f32 v[120:121], v[114:115], v[132:133]
	v_pk_mul_f32 v[114:115], v[114:115], v[132:133] op_sel:[1,0] op_sel_hi:[0,1]
	v_sub_f32_e32 v120, v120, v121
	v_add_f32_e32 v114, v114, v115
	v_pk_mul_f32 v[122:123], v[116:117], v[134:135]
	v_cvt_pk_bf16_f32 v120, v120, v114
	v_pk_mul_f32 v[114:115], v[116:117], v[134:135] op_sel:[1,0] op_sel_hi:[0,1]
	v_sub_f32_e32 v121, v122, v123
	v_add_f32_e32 v114, v114, v115
	v_cvt_pk_bf16_f32 v121, v121, v114
	global_store_dwordx4 v[164:165], v[118:121], off offset:256 nt
	v_mov_b32_e32 v132, 1.0
	v_mov_b32_e32 v133, 0
	v_or_b32_e32 v118, 16, v162
	v_mov_b32_e32 v114, 1.0
	v_mov_b32_e32 v115, 0
	v_mov_b32_e32 v116, 1.0
	v_mov_b32_e32 v117, 0
	s_and_saveexec_b64 s[30:31], s[28:29]
	s_cbranch_execz .LBB0_234
	v_mad_i64_i32 v[114:115], s[34:35], v118, 40, v[148:149]
	v_lshl_add_u64 v[114:115], v[114:115], 3, s[12:13]
	v_mov_b64_e32 v[130:131], v[178:179]
	v_mov_b64_e32 v[132:133], v[180:181]
	s_nop 0
	v_mov_b64_e32 v[114:115], v[182:183]
	v_mov_b64_e32 v[116:117], v[184:185]
.LBB0_234:
	s_or_b64 exec, exec, s[30:31]
	v_mov_b64_e32 v[120:121], s[10:11]
	v_mad_i64_i32 v[118:119], s[30:31], v118, s53, v[120:121]
	v_pk_mul_f32 v[120:121], v[112:113], v[132:133]
	v_pk_mul_f32 v[122:123], v[110:111], v[130:131]
	v_pk_mul_f32 v[110:111], v[110:111], v[130:131] op_sel:[1,0] op_sel_hi:[0,1]
	v_pk_mul_f32 v[112:113], v[112:113], v[132:133] op_sel:[1,0] op_sel_hi:[0,1]
	v_add_f32_e32 v110, v110, v111
	v_sub_f32_e32 v111, v120, v121
	v_add_f32_e32 v112, v112, v113
	v_sub_f32_e32 v122, v122, v123
	v_cvt_pk_bf16_f32 v110, v122, v110
	v_cvt_pk_bf16_f32 v111, v111, v112
	v_pk_mul_f32 v[112:113], v[106:107], v[114:115]
	v_pk_mul_f32 v[106:107], v[106:107], v[114:115] op_sel:[1,0] op_sel_hi:[0,1]
	v_sub_f32_e32 v112, v112, v113
	v_add_f32_e32 v106, v106, v107
	v_pk_mul_f32 v[120:121], v[108:109], v[116:117]
	v_cvt_pk_bf16_f32 v112, v112, v106
	v_pk_mul_f32 v[106:107], v[108:109], v[116:117] op_sel:[1,0] op_sel_hi:[0,1]
	v_sub_f32_e32 v113, v120, v121
	v_add_f32_e32 v106, v106, v107
	v_cvt_pk_bf16_f32 v113, v113, v106
	v_pk_mul_f32 v[106:107], v[104:105], v[132:133]
	v_pk_mul_f32 v[108:109], v[102:103], v[130:131]
	v_pk_mul_f32 v[102:103], v[102:103], v[130:131] op_sel:[1,0] op_sel_hi:[0,1]
	v_pk_mul_f32 v[104:105], v[104:105], v[132:133] op_sel:[1,0] op_sel_hi:[0,1]
	v_lshl_add_u64 v[118:119], v[154:155], 1, v[118:119]
	v_add_f32_e32 v102, v102, v103
	v_sub_f32_e32 v103, v106, v107
	v_add_f32_e32 v104, v104, v105
	global_store_dwordx4 v[118:119], v[110:113], off nt
	v_sub_f32_e32 v108, v108, v109
	v_cvt_pk_bf16_f32 v102, v108, v102
	v_cvt_pk_bf16_f32 v103, v103, v104
	v_pk_mul_f32 v[104:105], v[98:99], v[114:115]
	v_pk_mul_f32 v[98:99], v[98:99], v[114:115] op_sel:[1,0] op_sel_hi:[0,1]
	v_pk_mul_f32 v[106:107], v[100:101], v[116:117]
	v_sub_f32_e32 v104, v104, v105
	v_add_f32_e32 v98, v98, v99
	v_cvt_pk_bf16_f32 v104, v104, v98
	v_sub_f32_e32 v105, v106, v107
	v_pk_mul_f32 v[98:99], v[100:101], v[116:117] op_sel:[1,0] op_sel_hi:[0,1]
	v_add_f32_e32 v98, v98, v99
	v_cvt_pk_bf16_f32 v105, v105, v98
	global_store_dwordx4 v[118:119], v[102:105], off offset:256 nt
	v_or_b32_e32 v108, 32, v162
	v_mov_b32_e32 v99, 0
	v_mov_b32_e32 v98, 1.0
	v_mov_b32_e32 v104, 1.0
	v_mov_b32_e32 v105, 0
	v_mov_b32_e32 v106, 1.0
	v_mov_b32_e32 v107, 0
	v_mov_b32_e32 v100, 1.0
	v_mov_b32_e32 v101, 0
	v_mov_b32_e32 v102, 1.0
	v_mov_b32_e32 v103, 0
	s_and_saveexec_b64 s[30:31], s[28:29]
	s_cbranch_execz .LBB0_236
	v_mad_i64_i32 v[100:101], s[34:35], v108, 40, v[148:149]
	v_lshl_add_u64 v[100:101], v[100:101], 3, s[12:13]
	v_mov_b64_e32 v[104:105], v[186:187]
	v_mov_b64_e32 v[106:107], v[188:189]
	s_nop 0
	v_mov_b64_e32 v[100:101], v[190:191]
	v_mov_b64_e32 v[102:103], v[192:193]
.LBB0_236:
	s_or_b64 exec, exec, s[30:31]
	v_mov_b64_e32 v[110:111], s[10:11]
	v_mad_i64_i32 v[108:109], s[30:31], v108, s53, v[110:111]
	v_pk_mul_f32 v[110:111], v[96:97], v[106:107]
	v_pk_mul_f32 v[112:113], v[94:95], v[104:105]
	v_pk_mul_f32 v[94:95], v[94:95], v[104:105] op_sel:[1,0] op_sel_hi:[0,1]
	v_pk_mul_f32 v[96:97], v[96:97], v[106:107] op_sel:[1,0] op_sel_hi:[0,1]
	v_add_f32_e32 v94, v94, v95
	v_sub_f32_e32 v95, v110, v111
	v_add_f32_e32 v96, v96, v97
	v_sub_f32_e32 v112, v112, v113
	v_cvt_pk_bf16_f32 v94, v112, v94
	v_cvt_pk_bf16_f32 v95, v95, v96
	v_pk_mul_f32 v[96:97], v[90:91], v[100:101]
	v_pk_mul_f32 v[90:91], v[90:91], v[100:101] op_sel:[1,0] op_sel_hi:[0,1]
	v_sub_f32_e32 v96, v96, v97
	v_add_f32_e32 v90, v90, v91
	v_pk_mul_f32 v[110:111], v[92:93], v[102:103]
	v_cvt_pk_bf16_f32 v96, v96, v90
	v_pk_mul_f32 v[90:91], v[92:93], v[102:103] op_sel:[1,0] op_sel_hi:[0,1]
	v_sub_f32_e32 v97, v110, v111
	v_add_f32_e32 v90, v90, v91
	v_cvt_pk_bf16_f32 v97, v97, v90
	v_pk_mul_f32 v[90:91], v[88:89], v[106:107]
	v_pk_mul_f32 v[92:93], v[86:87], v[104:105]
	v_pk_mul_f32 v[86:87], v[86:87], v[104:105] op_sel:[1,0] op_sel_hi:[0,1]
	v_pk_mul_f32 v[88:89], v[88:89], v[106:107] op_sel:[1,0] op_sel_hi:[0,1]
	v_lshl_add_u64 v[108:109], v[154:155], 1, v[108:109]
	v_add_f32_e32 v86, v86, v87
	v_sub_f32_e32 v87, v90, v91
	v_add_f32_e32 v88, v88, v89
	global_store_dwordx4 v[108:109], v[94:97], off nt
	v_sub_f32_e32 v92, v92, v93
	v_cvt_pk_bf16_f32 v86, v92, v86
	v_cvt_pk_bf16_f32 v87, v87, v88
	v_pk_mul_f32 v[88:89], v[82:83], v[100:101]
	v_pk_mul_f32 v[82:83], v[82:83], v[100:101] op_sel:[1,0] op_sel_hi:[0,1]
	v_sub_f32_e32 v88, v88, v89
	v_add_f32_e32 v82, v82, v83
	v_pk_mul_f32 v[90:91], v[84:85], v[102:103]
	v_cvt_pk_bf16_f32 v88, v88, v82
	v_pk_mul_f32 v[82:83], v[84:85], v[102:103] op_sel:[1,0] op_sel_hi:[0,1]
	v_sub_f32_e32 v89, v90, v91
	v_add_f32_e32 v82, v82, v83
	v_cvt_pk_bf16_f32 v89, v89, v82
	global_store_dwordx4 v[108:109], v[86:89], off offset:256 nt
	v_mov_b32_e32 v100, 1.0
	v_mov_b32_e32 v101, 0
	v_or_b32_e32 v86, 48, v162
	v_mov_b32_e32 v82, 1.0
	v_mov_b32_e32 v83, 0
	v_mov_b32_e32 v84, 1.0
	v_mov_b32_e32 v85, 0
	s_and_saveexec_b64 s[30:31], s[28:29]
	s_cbranch_execz .LBB0_238
	v_mad_i64_i32 v[82:83], s[34:35], v86, 40, v[148:149]
	v_lshl_add_u64 v[82:83], v[82:83], 3, s[12:13]
	v_mov_b64_e32 v[98:99], v[194:195]
	v_mov_b64_e32 v[100:101], v[196:197]
	s_nop 0
	v_mov_b64_e32 v[82:83], v[198:199]
	v_mov_b64_e32 v[84:85], v[200:201]
.LBB0_238:
	s_or_b64 exec, exec, s[30:31]
	v_mov_b64_e32 v[88:89], s[10:11]
	v_mad_i64_i32 v[86:87], s[30:31], v86, s53, v[88:89]
	v_pk_mul_f32 v[88:89], v[80:81], v[100:101]
	v_pk_mul_f32 v[90:91], v[78:79], v[98:99]
	v_pk_mul_f32 v[78:79], v[78:79], v[98:99] op_sel:[1,0] op_sel_hi:[0,1]
	v_pk_mul_f32 v[80:81], v[80:81], v[100:101] op_sel:[1,0] op_sel_hi:[0,1]
	v_add_f32_e32 v78, v78, v79
	v_sub_f32_e32 v79, v88, v89
	v_add_f32_e32 v80, v80, v81
	v_sub_f32_e32 v90, v90, v91
	v_cvt_pk_bf16_f32 v78, v90, v78
	v_cvt_pk_bf16_f32 v79, v79, v80
	v_pk_mul_f32 v[80:81], v[74:75], v[82:83]
	v_pk_mul_f32 v[74:75], v[74:75], v[82:83] op_sel:[1,0] op_sel_hi:[0,1]
	v_sub_f32_e32 v80, v80, v81
	v_add_f32_e32 v74, v74, v75
	v_pk_mul_f32 v[88:89], v[76:77], v[84:85]
	v_cvt_pk_bf16_f32 v80, v80, v74
	v_pk_mul_f32 v[74:75], v[76:77], v[84:85] op_sel:[1,0] op_sel_hi:[0,1]
	v_sub_f32_e32 v81, v88, v89
	v_add_f32_e32 v74, v74, v75
	v_cvt_pk_bf16_f32 v81, v81, v74
	v_pk_mul_f32 v[74:75], v[72:73], v[100:101]
	v_pk_mul_f32 v[76:77], v[70:71], v[98:99]
	v_pk_mul_f32 v[70:71], v[70:71], v[98:99] op_sel:[1,0] op_sel_hi:[0,1]
	v_pk_mul_f32 v[72:73], v[72:73], v[100:101] op_sel:[1,0] op_sel_hi:[0,1]
	v_lshl_add_u64 v[86:87], v[154:155], 1, v[86:87]
	v_add_f32_e32 v70, v70, v71
	v_sub_f32_e32 v71, v74, v75
	v_add_f32_e32 v72, v72, v73
	global_store_dwordx4 v[86:87], v[78:81], off nt
	v_sub_f32_e32 v76, v76, v77
	v_cvt_pk_bf16_f32 v70, v76, v70
	v_cvt_pk_bf16_f32 v71, v71, v72
	v_pk_mul_f32 v[72:73], v[66:67], v[82:83]
	v_pk_mul_f32 v[66:67], v[66:67], v[82:83] op_sel:[1,0] op_sel_hi:[0,1]
	v_pk_mul_f32 v[74:75], v[68:69], v[84:85]
	v_sub_f32_e32 v72, v72, v73
	v_add_f32_e32 v66, v66, v67
	v_cvt_pk_bf16_f32 v72, v72, v66
	v_sub_f32_e32 v73, v74, v75
	v_pk_mul_f32 v[66:67], v[68:69], v[84:85] op_sel:[1,0] op_sel_hi:[0,1]
	v_add_f32_e32 v66, v66, v67
	v_cvt_pk_bf16_f32 v73, v73, v66
	global_store_dwordx4 v[86:87], v[70:73], off offset:256 nt
	v_add_u32_e32 v76, 0x80, v162
	v_mov_b32_e32 v67, 0
	v_mov_b32_e32 v66, 1.0
	v_mov_b32_e32 v72, 1.0
	v_mov_b32_e32 v73, 0
	v_mov_b32_e32 v74, 1.0
	v_mov_b32_e32 v75, 0
	v_mov_b32_e32 v68, 1.0
	v_mov_b32_e32 v69, 0
	v_mov_b32_e32 v70, 1.0
	v_mov_b32_e32 v71, 0
	s_and_saveexec_b64 s[30:31], s[28:29]
	s_cbranch_execz .LBB0_240
	v_mad_i64_i32 v[68:69], s[34:35], v76, 40, v[148:149]
	v_lshl_add_u64 v[68:69], v[68:69], 3, s[12:13]
	v_mov_b64_e32 v[72:73], v[202:203]
	v_mov_b64_e32 v[74:75], v[204:205]
	s_nop 0
	v_mov_b64_e32 v[68:69], v[206:207]
	v_mov_b64_e32 v[70:71], v[208:209]
.LBB0_240:
	s_or_b64 exec, exec, s[30:31]
	v_mov_b64_e32 v[78:79], s[10:11]
	v_mad_i64_i32 v[76:77], s[30:31], v76, s53, v[78:79]
	v_pk_mul_f32 v[78:79], v[64:65], v[74:75]
	v_pk_mul_f32 v[80:81], v[62:63], v[72:73]
	v_pk_mul_f32 v[62:63], v[62:63], v[72:73] op_sel:[1,0] op_sel_hi:[0,1]
	v_pk_mul_f32 v[64:65], v[64:65], v[74:75] op_sel:[1,0] op_sel_hi:[0,1]
	v_add_f32_e32 v62, v62, v63
	v_sub_f32_e32 v63, v78, v79
	v_add_f32_e32 v64, v64, v65
	v_sub_f32_e32 v80, v80, v81
	v_cvt_pk_bf16_f32 v62, v80, v62
	v_cvt_pk_bf16_f32 v63, v63, v64
	v_pk_mul_f32 v[64:65], v[58:59], v[68:69]
	v_pk_mul_f32 v[58:59], v[58:59], v[68:69] op_sel:[1,0] op_sel_hi:[0,1]
	v_sub_f32_e32 v64, v64, v65
	v_add_f32_e32 v58, v58, v59
	v_pk_mul_f32 v[78:79], v[60:61], v[70:71]
	v_cvt_pk_bf16_f32 v64, v64, v58
	v_pk_mul_f32 v[58:59], v[60:61], v[70:71] op_sel:[1,0] op_sel_hi:[0,1]
	v_sub_f32_e32 v65, v78, v79
	v_add_f32_e32 v58, v58, v59
	v_cvt_pk_bf16_f32 v65, v65, v58
	v_pk_mul_f32 v[58:59], v[56:57], v[74:75]
	v_pk_mul_f32 v[60:61], v[54:55], v[72:73]
	v_pk_mul_f32 v[54:55], v[54:55], v[72:73] op_sel:[1,0] op_sel_hi:[0,1]
	v_pk_mul_f32 v[56:57], v[56:57], v[74:75] op_sel:[1,0] op_sel_hi:[0,1]
	v_lshl_add_u64 v[76:77], v[154:155], 1, v[76:77]
	v_add_f32_e32 v54, v54, v55
	v_sub_f32_e32 v55, v58, v59
	v_add_f32_e32 v56, v56, v57
	global_store_dwordx4 v[76:77], v[62:65], off nt
	v_sub_f32_e32 v60, v60, v61
	v_cvt_pk_bf16_f32 v54, v60, v54
	v_cvt_pk_bf16_f32 v55, v55, v56
	v_pk_mul_f32 v[56:57], v[50:51], v[68:69]
	v_pk_mul_f32 v[50:51], v[50:51], v[68:69] op_sel:[1,0] op_sel_hi:[0,1]
	v_sub_f32_e32 v56, v56, v57
	v_add_f32_e32 v50, v50, v51
	v_pk_mul_f32 v[58:59], v[52:53], v[70:71]
	v_cvt_pk_bf16_f32 v56, v56, v50
	v_pk_mul_f32 v[50:51], v[52:53], v[70:71] op_sel:[1,0] op_sel_hi:[0,1]
	v_sub_f32_e32 v57, v58, v59
	v_add_f32_e32 v50, v50, v51
	v_cvt_pk_bf16_f32 v57, v57, v50
	global_store_dwordx4 v[76:77], v[54:57], off offset:256 nt
	v_mov_b32_e32 v68, 1.0
	v_mov_b32_e32 v69, 0
	v_add_u32_e32 v54, 0x90, v162
	v_mov_b32_e32 v50, 1.0
	v_mov_b32_e32 v51, 0
	v_mov_b32_e32 v52, 1.0
	v_mov_b32_e32 v53, 0
	s_and_saveexec_b64 s[30:31], s[28:29]
	s_cbranch_execz .LBB0_242
	v_mad_i64_i32 v[50:51], s[34:35], v54, 40, v[148:149]
	v_lshl_add_u64 v[50:51], v[50:51], 3, s[12:13]
	v_mov_b64_e32 v[66:67], v[210:211]
	v_mov_b64_e32 v[68:69], v[212:213]
	s_nop 0
	v_mov_b64_e32 v[50:51], v[214:215]
	v_mov_b64_e32 v[52:53], v[216:217]
.LBB0_242:
	s_or_b64 exec, exec, s[30:31]
	v_mov_b64_e32 v[56:57], s[10:11]
	v_mad_i64_i32 v[54:55], s[30:31], v54, s53, v[56:57]
	v_pk_mul_f32 v[56:57], v[48:49], v[68:69]
	v_pk_mul_f32 v[58:59], v[46:47], v[66:67]
	v_pk_mul_f32 v[46:47], v[46:47], v[66:67] op_sel:[1,0] op_sel_hi:[0,1]
	v_pk_mul_f32 v[48:49], v[48:49], v[68:69] op_sel:[1,0] op_sel_hi:[0,1]
	v_add_f32_e32 v46, v46, v47
	v_sub_f32_e32 v47, v56, v57
	v_add_f32_e32 v48, v48, v49
	v_sub_f32_e32 v58, v58, v59
	v_cvt_pk_bf16_f32 v46, v58, v46
	v_cvt_pk_bf16_f32 v47, v47, v48
	v_pk_mul_f32 v[48:49], v[42:43], v[50:51]
	v_pk_mul_f32 v[42:43], v[42:43], v[50:51] op_sel:[1,0] op_sel_hi:[0,1]
	v_sub_f32_e32 v48, v48, v49
	v_add_f32_e32 v42, v42, v43
	v_pk_mul_f32 v[56:57], v[44:45], v[52:53]
	v_cvt_pk_bf16_f32 v48, v48, v42
	v_pk_mul_f32 v[42:43], v[44:45], v[52:53] op_sel:[1,0] op_sel_hi:[0,1]
	v_sub_f32_e32 v49, v56, v57
	v_add_f32_e32 v42, v42, v43
	v_cvt_pk_bf16_f32 v49, v49, v42
	v_pk_mul_f32 v[42:43], v[40:41], v[68:69]
	v_pk_mul_f32 v[44:45], v[38:39], v[66:67]
	v_pk_mul_f32 v[38:39], v[38:39], v[66:67] op_sel:[1,0] op_sel_hi:[0,1]
	v_pk_mul_f32 v[40:41], v[40:41], v[68:69] op_sel:[1,0] op_sel_hi:[0,1]
	v_lshl_add_u64 v[54:55], v[154:155], 1, v[54:55]
	v_add_f32_e32 v38, v38, v39
	v_sub_f32_e32 v39, v42, v43
	v_add_f32_e32 v40, v40, v41
	global_store_dwordx4 v[54:55], v[46:49], off nt
	v_sub_f32_e32 v44, v44, v45
	v_cvt_pk_bf16_f32 v38, v44, v38
	v_cvt_pk_bf16_f32 v39, v39, v40
	v_pk_mul_f32 v[40:41], v[34:35], v[50:51]
	v_pk_mul_f32 v[34:35], v[34:35], v[50:51] op_sel:[1,0] op_sel_hi:[0,1]
	v_pk_mul_f32 v[42:43], v[36:37], v[52:53]
	v_sub_f32_e32 v40, v40, v41
	v_add_f32_e32 v34, v34, v35
	v_cvt_pk_bf16_f32 v40, v40, v34
	v_sub_f32_e32 v41, v42, v43
	v_pk_mul_f32 v[34:35], v[36:37], v[52:53] op_sel:[1,0] op_sel_hi:[0,1]
	v_add_f32_e32 v34, v34, v35
	v_cvt_pk_bf16_f32 v41, v41, v34
	global_store_dwordx4 v[54:55], v[38:41], off offset:256 nt
	v_add_u32_e32 v44, 0xa0, v162
	v_mov_b32_e32 v35, 0
	v_mov_b32_e32 v34, 1.0
	v_mov_b32_e32 v40, 1.0
	v_mov_b32_e32 v41, 0
	v_mov_b32_e32 v42, 1.0
	v_mov_b32_e32 v43, 0
	v_mov_b32_e32 v36, 1.0
	v_mov_b32_e32 v37, 0
	v_mov_b32_e32 v38, 1.0
	v_mov_b32_e32 v39, 0
	s_and_saveexec_b64 s[30:31], s[28:29]
	s_cbranch_execz .LBB0_244
	v_mad_i64_i32 v[36:37], s[34:35], v44, 40, v[148:149]
	v_lshl_add_u64 v[36:37], v[36:37], 3, s[12:13]
	v_mov_b64_e32 v[40:41], v[218:219]
	v_mov_b64_e32 v[42:43], v[220:221]
	s_nop 0
	v_mov_b64_e32 v[36:37], v[222:223]
	v_mov_b64_e32 v[38:39], v[224:225]
.LBB0_244:
	s_or_b64 exec, exec, s[30:31]
	v_mov_b64_e32 v[46:47], s[10:11]
	v_mad_i64_i32 v[44:45], s[30:31], v44, s53, v[46:47]
	v_pk_mul_f32 v[46:47], v[32:33], v[42:43]
	v_pk_mul_f32 v[48:49], v[30:31], v[40:41]
	v_pk_mul_f32 v[30:31], v[30:31], v[40:41] op_sel:[1,0] op_sel_hi:[0,1]
	v_pk_mul_f32 v[32:33], v[32:33], v[42:43] op_sel:[1,0] op_sel_hi:[0,1]
	v_add_f32_e32 v30, v30, v31
	v_sub_f32_e32 v31, v46, v47
	v_add_f32_e32 v32, v32, v33
	v_sub_f32_e32 v48, v48, v49
	v_cvt_pk_bf16_f32 v30, v48, v30
	v_cvt_pk_bf16_f32 v31, v31, v32
	v_pk_mul_f32 v[32:33], v[26:27], v[36:37]
	v_pk_mul_f32 v[26:27], v[26:27], v[36:37] op_sel:[1,0] op_sel_hi:[0,1]
	v_sub_f32_e32 v32, v32, v33
	v_add_f32_e32 v26, v26, v27
	v_pk_mul_f32 v[46:47], v[28:29], v[38:39]
	v_cvt_pk_bf16_f32 v32, v32, v26
	v_pk_mul_f32 v[26:27], v[28:29], v[38:39] op_sel:[1,0] op_sel_hi:[0,1]
	v_sub_f32_e32 v33, v46, v47
	v_add_f32_e32 v26, v26, v27
	v_cvt_pk_bf16_f32 v33, v33, v26
	v_pk_mul_f32 v[26:27], v[24:25], v[42:43]
	v_pk_mul_f32 v[28:29], v[22:23], v[40:41]
	v_pk_mul_f32 v[22:23], v[22:23], v[40:41] op_sel:[1,0] op_sel_hi:[0,1]
	v_pk_mul_f32 v[24:25], v[24:25], v[42:43] op_sel:[1,0] op_sel_hi:[0,1]
	v_lshl_add_u64 v[44:45], v[154:155], 1, v[44:45]
	v_add_f32_e32 v22, v22, v23
	v_sub_f32_e32 v23, v26, v27
	v_add_f32_e32 v24, v24, v25
	global_store_dwordx4 v[44:45], v[30:33], off nt
	v_sub_f32_e32 v28, v28, v29
	v_cvt_pk_bf16_f32 v22, v28, v22
	v_cvt_pk_bf16_f32 v23, v23, v24
	v_pk_mul_f32 v[24:25], v[18:19], v[36:37]
	v_pk_mul_f32 v[18:19], v[18:19], v[36:37] op_sel:[1,0] op_sel_hi:[0,1]
	v_sub_f32_e32 v24, v24, v25
	v_add_f32_e32 v18, v18, v19
	v_pk_mul_f32 v[26:27], v[20:21], v[38:39]
	v_cvt_pk_bf16_f32 v24, v24, v18
	v_pk_mul_f32 v[18:19], v[20:21], v[38:39] op_sel:[1,0] op_sel_hi:[0,1]
	v_sub_f32_e32 v25, v26, v27
	v_add_f32_e32 v18, v18, v19
	v_cvt_pk_bf16_f32 v25, v25, v18
	global_store_dwordx4 v[44:45], v[22:25], off offset:256 nt
	v_mov_b32_e32 v36, 1.0
	v_mov_b32_e32 v37, 0
	v_add_u32_e32 v22, 0xb0, v162
	v_mov_b32_e32 v18, 1.0
	v_mov_b32_e32 v19, 0
	v_mov_b32_e32 v20, 1.0
	v_mov_b32_e32 v21, 0
	s_and_saveexec_b64 s[30:31], s[28:29]
	s_cbranch_execz .LBB0_246
	v_mad_i64_i32 v[18:19], s[28:29], v22, 40, v[148:149]
	v_lshl_add_u64 v[18:19], v[18:19], 3, s[12:13]
	v_mov_b64_e32 v[34:35], v[226:227]
	v_mov_b64_e32 v[36:37], v[228:229]
	s_nop 0
	v_mov_b64_e32 v[18:19], v[234:235]
	v_mov_b64_e32 v[20:21], v[236:237]
.LBB0_246:
	s_or_b64 exec, exec, s[30:31]
	v_mov_b64_e32 v[24:25], s[10:11]
	v_mad_i64_i32 v[22:23], s[28:29], v22, s53, v[24:25]
	v_pk_mul_f32 v[24:25], v[16:17], v[36:37]
	v_pk_mul_f32 v[26:27], v[14:15], v[34:35]
	v_pk_mul_f32 v[14:15], v[14:15], v[34:35] op_sel:[1,0] op_sel_hi:[0,1]
	v_pk_mul_f32 v[16:17], v[16:17], v[36:37] op_sel:[1,0] op_sel_hi:[0,1]
	v_add_f32_e32 v14, v14, v15
	v_sub_f32_e32 v15, v24, v25
	v_add_f32_e32 v16, v16, v17
	v_sub_f32_e32 v26, v26, v27
	v_cvt_pk_bf16_f32 v14, v26, v14
	v_cvt_pk_bf16_f32 v15, v15, v16
	v_pk_mul_f32 v[16:17], v[10:11], v[18:19]
	v_pk_mul_f32 v[10:11], v[10:11], v[18:19] op_sel:[1,0] op_sel_hi:[0,1]
	v_sub_f32_e32 v16, v16, v17
	v_add_f32_e32 v10, v10, v11
	v_pk_mul_f32 v[24:25], v[12:13], v[20:21]
	v_cvt_pk_bf16_f32 v16, v16, v10
	v_pk_mul_f32 v[10:11], v[12:13], v[20:21] op_sel:[1,0] op_sel_hi:[0,1]
	v_sub_f32_e32 v17, v24, v25
	v_add_f32_e32 v10, v10, v11
	v_cvt_pk_bf16_f32 v17, v17, v10
	v_pk_mul_f32 v[10:11], v[8:9], v[36:37]
	v_pk_mul_f32 v[12:13], v[6:7], v[34:35]
	v_pk_mul_f32 v[6:7], v[6:7], v[34:35] op_sel:[1,0] op_sel_hi:[0,1]
	v_pk_mul_f32 v[8:9], v[8:9], v[36:37] op_sel:[1,0] op_sel_hi:[0,1]
	v_lshl_add_u64 v[22:23], v[154:155], 1, v[22:23]
	v_add_f32_e32 v6, v6, v7
	v_sub_f32_e32 v7, v10, v11
	v_add_f32_e32 v8, v8, v9
	global_store_dwordx4 v[22:23], v[14:17], off nt
	v_sub_f32_e32 v12, v12, v13
	v_cvt_pk_bf16_f32 v6, v12, v6
	v_cvt_pk_bf16_f32 v7, v7, v8
	v_pk_mul_f32 v[8:9], v[2:3], v[18:19]
	v_pk_mul_f32 v[2:3], v[2:3], v[18:19] op_sel:[1,0] op_sel_hi:[0,1]
	v_pk_mul_f32 v[10:11], v[4:5], v[20:21]
	v_sub_f32_e32 v8, v8, v9
	v_add_f32_e32 v2, v2, v3
	v_cvt_pk_bf16_f32 v8, v8, v2
	v_sub_f32_e32 v9, v10, v11
	v_pk_mul_f32 v[2:3], v[4:5], v[20:21] op_sel:[1,0] op_sel_hi:[0,1]
	s_andn2_b64 vcc, exec, s[22:23]
	s_mov_b64 s[22:23], -1
	v_add_f32_e32 v2, v2, v3
	v_cvt_pk_bf16_f32 v9, v9, v2
	global_store_dwordx4 v[22:23], v[6:9], off offset:256 nt
	s_cbranch_vccnz .LBB0_223
	s_andn2_b64 vcc, exec, s[8:9]
	s_cbranch_vccnz .LBB0_222
	s_barrier
	s_branch .LBB0_222

.LBB0_2548:
	v_lshl_or_b32 v154, s30, 8, v158
	s_and_b32 s2, s30, -4
	s_cmp_eq_u32 s2, 20
	v_and_b32_e32 v130, 56, v154
	s_cselect_b64 s[2:3], -1, 0
	v_cmp_gt_u32_e32 vcc, 16, v130
	s_and_b64 s[2:3], s[2:3], vcc
	s_cmp_lt_i32 s30, 4
	s_cselect_b64 s[30:31], -1, 0
	v_lshl_add_u32 v162, s34, 8, v156
	s_and_b64 s[34:35], s[30:31], exec
	s_cselect_b32 s21, 0, 32
	v_lshrrev_b32_e32 v130, 1, v130
	s_or_b64 s[30:31], s[30:31], s[2:3]
	v_or_b32_e32 v148, s21, v130
	v_mov_b32_e32 v131, 0
	v_mov_b32_e32 v130, 1.0
	v_mov_b32_e32 v136, 1.0
	v_mov_b32_e32 v137, 0
	v_mov_b32_e32 v138, 1.0
	v_mov_b32_e32 v139, 0
	v_mov_b32_e32 v132, 1.0
	v_mov_b32_e32 v133, 0
	v_mov_b32_e32 v134, 1.0
	v_mov_b32_e32 v135, 0
	s_and_saveexec_b64 s[34:35], s[30:31]
	s_cbranch_execz .Lg1pre_skip_L1
	v_mad_i64_i32 v[238:239], s[2:3], v162, 40, v[148:149]
	v_lshl_add_u64 v[238:239], v[238:239], 3, s[14:15]
	global_load_dwordx4 v[170:173], v[238:239], off
	global_load_dwordx4 v[174:177], v[238:239], off offset:16
	v_add_u32_e32 v238, 0x10, v162
	v_mad_i64_i32 v[238:239], s[2:3], v238, 40, v[148:149]
	v_lshl_add_u64 v[238:239], v[238:239], 3, s[14:15]
	global_load_dwordx4 v[178:181], v[238:239], off
	global_load_dwordx4 v[182:185], v[238:239], off offset:16
	v_add_u32_e32 v238, 0x20, v162
	v_mad_i64_i32 v[238:239], s[2:3], v238, 40, v[148:149]
	v_lshl_add_u64 v[238:239], v[238:239], 3, s[14:15]
	global_load_dwordx4 v[186:189], v[238:239], off
	global_load_dwordx4 v[190:193], v[238:239], off offset:16
	v_add_u32_e32 v238, 0x30, v162
	v_mad_i64_i32 v[238:239], s[2:3], v238, 40, v[148:149]
	v_lshl_add_u64 v[238:239], v[238:239], 3, s[14:15]
	global_load_dwordx4 v[194:197], v[238:239], off
	global_load_dwordx4 v[198:201], v[238:239], off offset:16
	v_add_u32_e32 v238, 0x80, v162
	v_mad_i64_i32 v[238:239], s[2:3], v238, 40, v[148:149]
	v_lshl_add_u64 v[238:239], v[238:239], 3, s[14:15]
	global_load_dwordx4 v[202:205], v[238:239], off
	global_load_dwordx4 v[206:209], v[238:239], off offset:16
	v_add_u32_e32 v238, 0x90, v162
	v_mad_i64_i32 v[238:239], s[2:3], v238, 40, v[148:149]
	v_lshl_add_u64 v[238:239], v[238:239], 3, s[14:15]
	global_load_dwordx4 v[210:213], v[238:239], off
	global_load_dwordx4 v[214:217], v[238:239], off offset:16
	v_add_u32_e32 v238, 0xa0, v162
	v_mad_i64_i32 v[238:239], s[2:3], v238, 40, v[148:149]
	v_lshl_add_u64 v[238:239], v[238:239], 3, s[14:15]
	global_load_dwordx4 v[218:221], v[238:239], off
	global_load_dwordx4 v[222:225], v[238:239], off offset:16
	v_add_u32_e32 v238, 0xb0, v162
	v_mad_i64_i32 v[238:239], s[2:3], v238, 40, v[148:149]
	v_lshl_add_u64 v[238:239], v[238:239], 3, s[14:15]
	global_load_dwordx4 v[226:229], v[238:239], off
	global_load_dwordx4 v[234:237], v[238:239], off offset:16
.Lg1pre_skip_L1:
	s_or_b64 exec, exec, s[34:35]
	s_waitcnt vmcnt(0)
	s_and_saveexec_b64 s[34:35], s[30:31]
	s_cbranch_execz .LBB0_2550
	v_mad_i64_i32 v[132:133], s[2:3], v162, 40, v[148:149]
	v_lshl_add_u64 v[132:133], v[132:133], 3, s[14:15]
	v_mov_b64_e32 v[136:137], v[170:171]
	v_mov_b64_e32 v[138:139], v[172:173]
	s_nop 0
	v_mov_b64_e32 v[132:133], v[174:175]
	v_mov_b64_e32 v[134:135], v[176:177]
.LBB0_2550:
	s_or_b64 exec, exec, s[34:35]
	s_waitcnt vmcnt(0)
	v_pk_mul_f32 v[166:167], v[128:129], v[138:139]
	v_pk_mul_f32 v[168:169], v[126:127], v[136:137]
	v_pk_mul_f32 v[126:127], v[126:127], v[136:137] op_sel:[1,0] op_sel_hi:[0,1]
	v_pk_mul_f32 v[128:129], v[128:129], v[138:139] op_sel:[1,0] op_sel_hi:[0,1]
	v_add_f32_e32 v126, v126, v127
	v_sub_f32_e32 v127, v166, v167
	v_add_f32_e32 v128, v128, v129
	v_sub_f32_e32 v163, v168, v169
	v_cvt_pk_bf16_f32 v126, v163, v126
	v_cvt_pk_bf16_f32 v127, v127, v128
	v_pk_mul_f32 v[128:129], v[122:123], v[132:133]
	v_pk_mul_f32 v[122:123], v[122:123], v[132:133] op_sel:[1,0] op_sel_hi:[0,1]
	v_sub_f32_e32 v128, v128, v129
	v_add_f32_e32 v122, v122, v123
	v_pk_mul_f32 v[166:167], v[124:125], v[134:135]
	v_cvt_pk_bf16_f32 v128, v128, v122
	v_pk_mul_f32 v[122:123], v[124:125], v[134:135] op_sel:[1,0] op_sel_hi:[0,1]
	v_mov_b64_e32 v[164:165], s[12:13]
	v_sub_f32_e32 v129, v166, v167
	v_add_f32_e32 v122, v122, v123
	v_ashrrev_i32_e32 v155, 31, v154
	v_mad_i64_i32 v[164:165], s[2:3], v162, s52, v[164:165]
	v_cvt_pk_bf16_f32 v129, v129, v122
	v_pk_mul_f32 v[122:123], v[120:121], v[138:139]
	v_pk_mul_f32 v[124:125], v[118:119], v[136:137]
	v_pk_mul_f32 v[118:119], v[118:119], v[136:137] op_sel:[1,0] op_sel_hi:[0,1]
	v_pk_mul_f32 v[120:121], v[120:121], v[138:139] op_sel:[1,0] op_sel_hi:[0,1]
	v_lshl_add_u64 v[164:165], v[154:155], 1, v[164:165]
	v_add_f32_e32 v118, v118, v119
	v_sub_f32_e32 v119, v122, v123
	v_add_f32_e32 v120, v120, v121
	global_store_dwordx4 v[164:165], v[126:129], off nt
	v_sub_f32_e32 v124, v124, v125
	v_cvt_pk_bf16_f32 v118, v124, v118
	v_cvt_pk_bf16_f32 v119, v119, v120
	v_pk_mul_f32 v[120:121], v[114:115], v[132:133]
	v_pk_mul_f32 v[114:115], v[114:115], v[132:133] op_sel:[1,0] op_sel_hi:[0,1]
	v_sub_f32_e32 v120, v120, v121
	v_add_f32_e32 v114, v114, v115
	v_pk_mul_f32 v[122:123], v[116:117], v[134:135]
	v_cvt_pk_bf16_f32 v120, v120, v114
	v_pk_mul_f32 v[114:115], v[116:117], v[134:135] op_sel:[1,0] op_sel_hi:[0,1]
	v_sub_f32_e32 v121, v122, v123
	v_add_f32_e32 v114, v114, v115
	v_cvt_pk_bf16_f32 v121, v121, v114
	global_store_dwordx4 v[164:165], v[118:121], off offset:256 nt
	v_mov_b32_e32 v132, 1.0
	v_mov_b32_e32 v133, 0
	v_or_b32_e32 v118, 16, v162
	v_mov_b32_e32 v114, 1.0
	v_mov_b32_e32 v115, 0
	v_mov_b32_e32 v116, 1.0
	v_mov_b32_e32 v117, 0
	s_and_saveexec_b64 s[34:35], s[30:31]
	s_cbranch_execz .LBB0_2552
	v_mad_i64_i32 v[114:115], s[2:3], v118, 40, v[148:149]
	v_lshl_add_u64 v[114:115], v[114:115], 3, s[14:15]
	v_mov_b64_e32 v[130:131], v[178:179]
	v_mov_b64_e32 v[132:133], v[180:181]
	s_nop 0
	v_mov_b64_e32 v[114:115], v[182:183]
	v_mov_b64_e32 v[116:117], v[184:185]
.LBB0_2552:
	s_or_b64 exec, exec, s[34:35]
	v_mov_b64_e32 v[120:121], s[12:13]
	v_mad_i64_i32 v[118:119], s[2:3], v118, s52, v[120:121]
	v_pk_mul_f32 v[120:121], v[112:113], v[132:133]
	v_pk_mul_f32 v[122:123], v[110:111], v[130:131]
	v_pk_mul_f32 v[110:111], v[110:111], v[130:131] op_sel:[1,0] op_sel_hi:[0,1]
	v_pk_mul_f32 v[112:113], v[112:113], v[132:133] op_sel:[1,0] op_sel_hi:[0,1]
	v_add_f32_e32 v110, v110, v111
	v_sub_f32_e32 v111, v120, v121
	v_add_f32_e32 v112, v112, v113
	v_sub_f32_e32 v122, v122, v123
	v_cvt_pk_bf16_f32 v110, v122, v110
	v_cvt_pk_bf16_f32 v111, v111, v112
	v_pk_mul_f32 v[112:113], v[106:107], v[114:115]
	v_pk_mul_f32 v[106:107], v[106:107], v[114:115] op_sel:[1,0] op_sel_hi:[0,1]
	v_sub_f32_e32 v112, v112, v113
	v_add_f32_e32 v106, v106, v107
	v_pk_mul_f32 v[120:121], v[108:109], v[116:117]
	v_cvt_pk_bf16_f32 v112, v112, v106
	v_pk_mul_f32 v[106:107], v[108:109], v[116:117] op_sel:[1,0] op_sel_hi:[0,1]
	v_sub_f32_e32 v113, v120, v121
	v_add_f32_e32 v106, v106, v107
	v_cvt_pk_bf16_f32 v113, v113, v106
	v_pk_mul_f32 v[106:107], v[104:105], v[132:133]
	v_pk_mul_f32 v[108:109], v[102:103], v[130:131]
	v_pk_mul_f32 v[102:103], v[102:103], v[130:131] op_sel:[1,0] op_sel_hi:[0,1]
	v_pk_mul_f32 v[104:105], v[104:105], v[132:133] op_sel:[1,0] op_sel_hi:[0,1]
	v_lshl_add_u64 v[118:119], v[154:155], 1, v[118:119]
	v_add_f32_e32 v102, v102, v103
	v_sub_f32_e32 v103, v106, v107
	v_add_f32_e32 v104, v104, v105
	global_store_dwordx4 v[118:119], v[110:113], off nt
	v_sub_f32_e32 v108, v108, v109
	v_cvt_pk_bf16_f32 v102, v108, v102
	v_cvt_pk_bf16_f32 v103, v103, v104
	v_pk_mul_f32 v[104:105], v[98:99], v[114:115]
	v_pk_mul_f32 v[98:99], v[98:99], v[114:115] op_sel:[1,0] op_sel_hi:[0,1]
	v_pk_mul_f32 v[106:107], v[100:101], v[116:117]
	v_sub_f32_e32 v104, v104, v105
	v_add_f32_e32 v98, v98, v99
	v_cvt_pk_bf16_f32 v104, v104, v98
	v_sub_f32_e32 v105, v106, v107
	v_pk_mul_f32 v[98:99], v[100:101], v[116:117] op_sel:[1,0] op_sel_hi:[0,1]
	v_add_f32_e32 v98, v98, v99
	v_cvt_pk_bf16_f32 v105, v105, v98
	global_store_dwordx4 v[118:119], v[102:105], off offset:256 nt
	v_or_b32_e32 v108, 32, v162
	v_mov_b32_e32 v99, 0
	v_mov_b32_e32 v98, 1.0
	v_mov_b32_e32 v104, 1.0
	v_mov_b32_e32 v105, 0
	v_mov_b32_e32 v106, 1.0
	v_mov_b32_e32 v107, 0
	v_mov_b32_e32 v100, 1.0
	v_mov_b32_e32 v101, 0
	v_mov_b32_e32 v102, 1.0
	v_mov_b32_e32 v103, 0
	s_and_saveexec_b64 s[34:35], s[30:31]
	s_cbranch_execz .LBB0_2554
	v_mad_i64_i32 v[100:101], s[2:3], v108, 40, v[148:149]
	v_lshl_add_u64 v[100:101], v[100:101], 3, s[14:15]
	v_mov_b64_e32 v[104:105], v[186:187]
	v_mov_b64_e32 v[106:107], v[188:189]
	s_nop 0
	v_mov_b64_e32 v[100:101], v[190:191]
	v_mov_b64_e32 v[102:103], v[192:193]
.LBB0_2554:
	s_or_b64 exec, exec, s[34:35]
	v_mov_b64_e32 v[110:111], s[12:13]
	v_mad_i64_i32 v[108:109], s[2:3], v108, s52, v[110:111]
	v_pk_mul_f32 v[110:111], v[96:97], v[106:107]
	v_pk_mul_f32 v[112:113], v[94:95], v[104:105]
	v_pk_mul_f32 v[94:95], v[94:95], v[104:105] op_sel:[1,0] op_sel_hi:[0,1]
	v_pk_mul_f32 v[96:97], v[96:97], v[106:107] op_sel:[1,0] op_sel_hi:[0,1]
	v_add_f32_e32 v94, v94, v95
	v_sub_f32_e32 v95, v110, v111
	v_add_f32_e32 v96, v96, v97
	v_sub_f32_e32 v112, v112, v113
	v_cvt_pk_bf16_f32 v94, v112, v94
	v_cvt_pk_bf16_f32 v95, v95, v96
	v_pk_mul_f32 v[96:97], v[90:91], v[100:101]
	v_pk_mul_f32 v[90:91], v[90:91], v[100:101] op_sel:[1,0] op_sel_hi:[0,1]
	v_sub_f32_e32 v96, v96, v97
	v_add_f32_e32 v90, v90, v91
	v_pk_mul_f32 v[110:111], v[92:93], v[102:103]
	v_cvt_pk_bf16_f32 v96, v96, v90
	v_pk_mul_f32 v[90:91], v[92:93], v[102:103] op_sel:[1,0] op_sel_hi:[0,1]
	v_sub_f32_e32 v97, v110, v111
	v_add_f32_e32 v90, v90, v91
	v_cvt_pk_bf16_f32 v97, v97, v90
	v_pk_mul_f32 v[90:91], v[88:89], v[106:107]
	v_pk_mul_f32 v[92:93], v[86:87], v[104:105]
	v_pk_mul_f32 v[86:87], v[86:87], v[104:105] op_sel:[1,0] op_sel_hi:[0,1]
	v_pk_mul_f32 v[88:89], v[88:89], v[106:107] op_sel:[1,0] op_sel_hi:[0,1]
	v_lshl_add_u64 v[108:109], v[154:155], 1, v[108:109]
	v_add_f32_e32 v86, v86, v87
	v_sub_f32_e32 v87, v90, v91
	v_add_f32_e32 v88, v88, v89
	global_store_dwordx4 v[108:109], v[94:97], off nt
	v_sub_f32_e32 v92, v92, v93
	v_cvt_pk_bf16_f32 v86, v92, v86
	v_cvt_pk_bf16_f32 v87, v87, v88
	v_pk_mul_f32 v[88:89], v[82:83], v[100:101]
	v_pk_mul_f32 v[82:83], v[82:83], v[100:101] op_sel:[1,0] op_sel_hi:[0,1]
	v_sub_f32_e32 v88, v88, v89
	v_add_f32_e32 v82, v82, v83
	v_pk_mul_f32 v[90:91], v[84:85], v[102:103]
	v_cvt_pk_bf16_f32 v88, v88, v82
	v_pk_mul_f32 v[82:83], v[84:85], v[102:103] op_sel:[1,0] op_sel_hi:[0,1]
	v_sub_f32_e32 v89, v90, v91
	v_add_f32_e32 v82, v82, v83
	v_cvt_pk_bf16_f32 v89, v89, v82
	global_store_dwordx4 v[108:109], v[86:89], off offset:256 nt
	v_mov_b32_e32 v100, 1.0
	v_mov_b32_e32 v101, 0
	v_or_b32_e32 v86, 48, v162
	v_mov_b32_e32 v82, 1.0
	v_mov_b32_e32 v83, 0
	v_mov_b32_e32 v84, 1.0
	v_mov_b32_e32 v85, 0
	s_and_saveexec_b64 s[34:35], s[30:31]
	s_cbranch_execz .LBB0_2556
	v_mad_i64_i32 v[82:83], s[2:3], v86, 40, v[148:149]
	v_lshl_add_u64 v[82:83], v[82:83], 3, s[14:15]
	v_mov_b64_e32 v[98:99], v[194:195]
	v_mov_b64_e32 v[100:101], v[196:197]
	s_nop 0
	v_mov_b64_e32 v[82:83], v[198:199]
	v_mov_b64_e32 v[84:85], v[200:201]
.LBB0_2556:
	s_or_b64 exec, exec, s[34:35]
	v_mov_b64_e32 v[88:89], s[12:13]
	v_mad_i64_i32 v[86:87], s[2:3], v86, s52, v[88:89]
	v_pk_mul_f32 v[88:89], v[80:81], v[100:101]
	v_pk_mul_f32 v[90:91], v[78:79], v[98:99]
	v_pk_mul_f32 v[78:79], v[78:79], v[98:99] op_sel:[1,0] op_sel_hi:[0,1]
	v_pk_mul_f32 v[80:81], v[80:81], v[100:101] op_sel:[1,0] op_sel_hi:[0,1]
	v_add_f32_e32 v78, v78, v79
	v_sub_f32_e32 v79, v88, v89
	v_add_f32_e32 v80, v80, v81
	v_sub_f32_e32 v90, v90, v91
	v_cvt_pk_bf16_f32 v78, v90, v78
	v_cvt_pk_bf16_f32 v79, v79, v80
	v_pk_mul_f32 v[80:81], v[74:75], v[82:83]
	v_pk_mul_f32 v[74:75], v[74:75], v[82:83] op_sel:[1,0] op_sel_hi:[0,1]
	v_sub_f32_e32 v80, v80, v81
	v_add_f32_e32 v74, v74, v75
	v_pk_mul_f32 v[88:89], v[76:77], v[84:85]
	v_cvt_pk_bf16_f32 v80, v80, v74
	v_pk_mul_f32 v[74:75], v[76:77], v[84:85] op_sel:[1,0] op_sel_hi:[0,1]
	v_sub_f32_e32 v81, v88, v89
	v_add_f32_e32 v74, v74, v75
	v_cvt_pk_bf16_f32 v81, v81, v74
	v_pk_mul_f32 v[74:75], v[72:73], v[100:101]
	v_pk_mul_f32 v[76:77], v[70:71], v[98:99]
	v_pk_mul_f32 v[70:71], v[70:71], v[98:99] op_sel:[1,0] op_sel_hi:[0,1]
	v_pk_mul_f32 v[72:73], v[72:73], v[100:101] op_sel:[1,0] op_sel_hi:[0,1]
	v_lshl_add_u64 v[86:87], v[154:155], 1, v[86:87]
	v_add_f32_e32 v70, v70, v71
	v_sub_f32_e32 v71, v74, v75
	v_add_f32_e32 v72, v72, v73
	global_store_dwordx4 v[86:87], v[78:81], off nt
	v_sub_f32_e32 v76, v76, v77
	v_cvt_pk_bf16_f32 v70, v76, v70
	v_cvt_pk_bf16_f32 v71, v71, v72
	v_pk_mul_f32 v[72:73], v[66:67], v[82:83]
	v_pk_mul_f32 v[66:67], v[66:67], v[82:83] op_sel:[1,0] op_sel_hi:[0,1]
	v_pk_mul_f32 v[74:75], v[68:69], v[84:85]
	v_sub_f32_e32 v72, v72, v73
	v_add_f32_e32 v66, v66, v67
	v_cvt_pk_bf16_f32 v72, v72, v66
	v_sub_f32_e32 v73, v74, v75
	v_pk_mul_f32 v[66:67], v[68:69], v[84:85] op_sel:[1,0] op_sel_hi:[0,1]
	v_add_f32_e32 v66, v66, v67
	v_cvt_pk_bf16_f32 v73, v73, v66
	global_store_dwordx4 v[86:87], v[70:73], off offset:256 nt
	v_add_u32_e32 v76, 0x80, v162
	v_mov_b32_e32 v67, 0
	v_mov_b32_e32 v66, 1.0
	v_mov_b32_e32 v72, 1.0
	v_mov_b32_e32 v73, 0
	v_mov_b32_e32 v74, 1.0
	v_mov_b32_e32 v75, 0
	v_mov_b32_e32 v68, 1.0
	v_mov_b32_e32 v69, 0
	v_mov_b32_e32 v70, 1.0
	v_mov_b32_e32 v71, 0
	s_and_saveexec_b64 s[34:35], s[30:31]
	s_cbranch_execz .LBB0_2558
	v_mad_i64_i32 v[68:69], s[2:3], v76, 40, v[148:149]
	v_lshl_add_u64 v[68:69], v[68:69], 3, s[14:15]
	v_mov_b64_e32 v[72:73], v[202:203]
	v_mov_b64_e32 v[74:75], v[204:205]
	s_nop 0
	v_mov_b64_e32 v[68:69], v[206:207]
	v_mov_b64_e32 v[70:71], v[208:209]
.LBB0_2558:
	s_or_b64 exec, exec, s[34:35]
	v_mov_b64_e32 v[78:79], s[12:13]
	v_mad_i64_i32 v[76:77], s[2:3], v76, s52, v[78:79]
	v_pk_mul_f32 v[78:79], v[64:65], v[74:75]
	v_pk_mul_f32 v[80:81], v[62:63], v[72:73]
	v_pk_mul_f32 v[62:63], v[62:63], v[72:73] op_sel:[1,0] op_sel_hi:[0,1]
	v_pk_mul_f32 v[64:65], v[64:65], v[74:75] op_sel:[1,0] op_sel_hi:[0,1]
	v_add_f32_e32 v62, v62, v63
	v_sub_f32_e32 v63, v78, v79
	v_add_f32_e32 v64, v64, v65
	v_sub_f32_e32 v80, v80, v81
	v_cvt_pk_bf16_f32 v62, v80, v62
	v_cvt_pk_bf16_f32 v63, v63, v64
	v_pk_mul_f32 v[64:65], v[58:59], v[68:69]
	v_pk_mul_f32 v[58:59], v[58:59], v[68:69] op_sel:[1,0] op_sel_hi:[0,1]
	v_sub_f32_e32 v64, v64, v65
	v_add_f32_e32 v58, v58, v59
	v_pk_mul_f32 v[78:79], v[60:61], v[70:71]
	v_cvt_pk_bf16_f32 v64, v64, v58
	v_pk_mul_f32 v[58:59], v[60:61], v[70:71] op_sel:[1,0] op_sel_hi:[0,1]
	v_sub_f32_e32 v65, v78, v79
	v_add_f32_e32 v58, v58, v59
	v_cvt_pk_bf16_f32 v65, v65, v58
	v_pk_mul_f32 v[58:59], v[56:57], v[74:75]
	v_pk_mul_f32 v[60:61], v[54:55], v[72:73]
	v_pk_mul_f32 v[54:55], v[54:55], v[72:73] op_sel:[1,0] op_sel_hi:[0,1]
	v_pk_mul_f32 v[56:57], v[56:57], v[74:75] op_sel:[1,0] op_sel_hi:[0,1]
	v_lshl_add_u64 v[76:77], v[154:155], 1, v[76:77]
	v_add_f32_e32 v54, v54, v55
	v_sub_f32_e32 v55, v58, v59
	v_add_f32_e32 v56, v56, v57
	global_store_dwordx4 v[76:77], v[62:65], off nt
	v_sub_f32_e32 v60, v60, v61
	v_cvt_pk_bf16_f32 v54, v60, v54
	v_cvt_pk_bf16_f32 v55, v55, v56
	v_pk_mul_f32 v[56:57], v[50:51], v[68:69]
	v_pk_mul_f32 v[50:51], v[50:51], v[68:69] op_sel:[1,0] op_sel_hi:[0,1]
	v_sub_f32_e32 v56, v56, v57
	v_add_f32_e32 v50, v50, v51
	v_pk_mul_f32 v[58:59], v[52:53], v[70:71]
	v_cvt_pk_bf16_f32 v56, v56, v50
	v_pk_mul_f32 v[50:51], v[52:53], v[70:71] op_sel:[1,0] op_sel_hi:[0,1]
	v_sub_f32_e32 v57, v58, v59
	v_add_f32_e32 v50, v50, v51
	v_cvt_pk_bf16_f32 v57, v57, v50
	global_store_dwordx4 v[76:77], v[54:57], off offset:256 nt
	v_mov_b32_e32 v68, 1.0
	v_mov_b32_e32 v69, 0
	v_add_u32_e32 v54, 0x90, v162
	v_mov_b32_e32 v50, 1.0
	v_mov_b32_e32 v51, 0
	v_mov_b32_e32 v52, 1.0
	v_mov_b32_e32 v53, 0
	s_and_saveexec_b64 s[34:35], s[30:31]
	s_cbranch_execz .LBB0_2560
	v_mad_i64_i32 v[50:51], s[2:3], v54, 40, v[148:149]
	v_lshl_add_u64 v[50:51], v[50:51], 3, s[14:15]
	v_mov_b64_e32 v[66:67], v[210:211]
	v_mov_b64_e32 v[68:69], v[212:213]
	s_nop 0
	v_mov_b64_e32 v[50:51], v[214:215]
	v_mov_b64_e32 v[52:53], v[216:217]
.LBB0_2560:
	s_or_b64 exec, exec, s[34:35]
	v_mov_b64_e32 v[56:57], s[12:13]
	v_mad_i64_i32 v[54:55], s[2:3], v54, s52, v[56:57]
	v_pk_mul_f32 v[56:57], v[48:49], v[68:69]
	v_pk_mul_f32 v[58:59], v[46:47], v[66:67]
	v_pk_mul_f32 v[46:47], v[46:47], v[66:67] op_sel:[1,0] op_sel_hi:[0,1]
	v_pk_mul_f32 v[48:49], v[48:49], v[68:69] op_sel:[1,0] op_sel_hi:[0,1]
	v_add_f32_e32 v46, v46, v47
	v_sub_f32_e32 v47, v56, v57
	v_add_f32_e32 v48, v48, v49
	v_sub_f32_e32 v58, v58, v59
	v_cvt_pk_bf16_f32 v46, v58, v46
	v_cvt_pk_bf16_f32 v47, v47, v48
	v_pk_mul_f32 v[48:49], v[42:43], v[50:51]
	v_pk_mul_f32 v[42:43], v[42:43], v[50:51] op_sel:[1,0] op_sel_hi:[0,1]
	v_sub_f32_e32 v48, v48, v49
	v_add_f32_e32 v42, v42, v43
	v_pk_mul_f32 v[56:57], v[44:45], v[52:53]
	v_cvt_pk_bf16_f32 v48, v48, v42
	v_pk_mul_f32 v[42:43], v[44:45], v[52:53] op_sel:[1,0] op_sel_hi:[0,1]
	v_sub_f32_e32 v49, v56, v57
	v_add_f32_e32 v42, v42, v43
	v_cvt_pk_bf16_f32 v49, v49, v42
	v_pk_mul_f32 v[42:43], v[40:41], v[68:69]
	v_pk_mul_f32 v[44:45], v[38:39], v[66:67]
	v_pk_mul_f32 v[38:39], v[38:39], v[66:67] op_sel:[1,0] op_sel_hi:[0,1]
	v_pk_mul_f32 v[40:41], v[40:41], v[68:69] op_sel:[1,0] op_sel_hi:[0,1]
	v_lshl_add_u64 v[54:55], v[154:155], 1, v[54:55]
	v_add_f32_e32 v38, v38, v39
	v_sub_f32_e32 v39, v42, v43
	v_add_f32_e32 v40, v40, v41
	global_store_dwordx4 v[54:55], v[46:49], off nt
	v_sub_f32_e32 v44, v44, v45
	v_cvt_pk_bf16_f32 v38, v44, v38
	v_cvt_pk_bf16_f32 v39, v39, v40
	v_pk_mul_f32 v[40:41], v[34:35], v[50:51]
	v_pk_mul_f32 v[34:35], v[34:35], v[50:51] op_sel:[1,0] op_sel_hi:[0,1]
	v_pk_mul_f32 v[42:43], v[36:37], v[52:53]
	v_sub_f32_e32 v40, v40, v41
	v_add_f32_e32 v34, v34, v35
	v_cvt_pk_bf16_f32 v40, v40, v34
	v_sub_f32_e32 v41, v42, v43
	v_pk_mul_f32 v[34:35], v[36:37], v[52:53] op_sel:[1,0] op_sel_hi:[0,1]
	v_add_f32_e32 v34, v34, v35
	v_cvt_pk_bf16_f32 v41, v41, v34
	global_store_dwordx4 v[54:55], v[38:41], off offset:256 nt
	v_add_u32_e32 v44, 0xa0, v162
	v_mov_b32_e32 v35, 0
	v_mov_b32_e32 v34, 1.0
	v_mov_b32_e32 v40, 1.0
	v_mov_b32_e32 v41, 0
	v_mov_b32_e32 v42, 1.0
	v_mov_b32_e32 v43, 0
	v_mov_b32_e32 v36, 1.0
	v_mov_b32_e32 v37, 0
	v_mov_b32_e32 v38, 1.0
	v_mov_b32_e32 v39, 0
	s_and_saveexec_b64 s[34:35], s[30:31]
	s_cbranch_execz .LBB0_2562
	v_mad_i64_i32 v[36:37], s[2:3], v44, 40, v[148:149]
	v_lshl_add_u64 v[36:37], v[36:37], 3, s[14:15]
	v_mov_b64_e32 v[40:41], v[218:219]
	v_mov_b64_e32 v[42:43], v[220:221]
	s_nop 0
	v_mov_b64_e32 v[36:37], v[222:223]
	v_mov_b64_e32 v[38:39], v[224:225]
.LBB0_2562:
	s_or_b64 exec, exec, s[34:35]
	v_mov_b64_e32 v[46:47], s[12:13]
	v_mad_i64_i32 v[44:45], s[2:3], v44, s52, v[46:47]
	v_pk_mul_f32 v[46:47], v[32:33], v[42:43]
	v_pk_mul_f32 v[48:49], v[30:31], v[40:41]
	v_pk_mul_f32 v[30:31], v[30:31], v[40:41] op_sel:[1,0] op_sel_hi:[0,1]
	v_pk_mul_f32 v[32:33], v[32:33], v[42:43] op_sel:[1,0] op_sel_hi:[0,1]
	v_add_f32_e32 v30, v30, v31
	v_sub_f32_e32 v31, v46, v47
	v_add_f32_e32 v32, v32, v33
	v_sub_f32_e32 v48, v48, v49
	v_cvt_pk_bf16_f32 v30, v48, v30
	v_cvt_pk_bf16_f32 v31, v31, v32
	v_pk_mul_f32 v[32:33], v[26:27], v[36:37]
	v_pk_mul_f32 v[26:27], v[26:27], v[36:37] op_sel:[1,0] op_sel_hi:[0,1]
	v_sub_f32_e32 v32, v32, v33
	v_add_f32_e32 v26, v26, v27
	v_pk_mul_f32 v[46:47], v[28:29], v[38:39]
	v_cvt_pk_bf16_f32 v32, v32, v26
	v_pk_mul_f32 v[26:27], v[28:29], v[38:39] op_sel:[1,0] op_sel_hi:[0,1]
	v_sub_f32_e32 v33, v46, v47
	v_add_f32_e32 v26, v26, v27
	v_cvt_pk_bf16_f32 v33, v33, v26
	v_pk_mul_f32 v[26:27], v[24:25], v[42:43]
	v_pk_mul_f32 v[28:29], v[22:23], v[40:41]
	v_pk_mul_f32 v[22:23], v[22:23], v[40:41] op_sel:[1,0] op_sel_hi:[0,1]
	v_pk_mul_f32 v[24:25], v[24:25], v[42:43] op_sel:[1,0] op_sel_hi:[0,1]
	v_lshl_add_u64 v[44:45], v[154:155], 1, v[44:45]
	v_add_f32_e32 v22, v22, v23
	v_sub_f32_e32 v23, v26, v27
	v_add_f32_e32 v24, v24, v25
	global_store_dwordx4 v[44:45], v[30:33], off nt
	v_sub_f32_e32 v28, v28, v29
	v_cvt_pk_bf16_f32 v22, v28, v22
	v_cvt_pk_bf16_f32 v23, v23, v24
	v_pk_mul_f32 v[24:25], v[18:19], v[36:37]
	v_pk_mul_f32 v[18:19], v[18:19], v[36:37] op_sel:[1,0] op_sel_hi:[0,1]
	v_sub_f32_e32 v24, v24, v25
	v_add_f32_e32 v18, v18, v19
	v_pk_mul_f32 v[26:27], v[20:21], v[38:39]
	v_cvt_pk_bf16_f32 v24, v24, v18
	v_pk_mul_f32 v[18:19], v[20:21], v[38:39] op_sel:[1,0] op_sel_hi:[0,1]
	v_sub_f32_e32 v25, v26, v27
	v_add_f32_e32 v18, v18, v19
	v_cvt_pk_bf16_f32 v25, v25, v18
	global_store_dwordx4 v[44:45], v[22:25], off offset:256 nt
	v_mov_b32_e32 v36, 1.0
	v_mov_b32_e32 v37, 0
	v_add_u32_e32 v22, 0xb0, v162
	v_mov_b32_e32 v18, 1.0
	v_mov_b32_e32 v19, 0
	v_mov_b32_e32 v20, 1.0
	v_mov_b32_e32 v21, 0
	s_and_saveexec_b64 s[34:35], s[30:31]
	s_cbranch_execz .LBB0_2564
	v_mad_i64_i32 v[18:19], s[2:3], v22, 40, v[148:149]
	v_lshl_add_u64 v[18:19], v[18:19], 3, s[14:15]
	v_mov_b64_e32 v[34:35], v[226:227]
	v_mov_b64_e32 v[36:37], v[228:229]
	s_nop 0
	v_mov_b64_e32 v[18:19], v[234:235]
	v_mov_b64_e32 v[20:21], v[236:237]
.LBB0_2564:
	s_or_b64 exec, exec, s[34:35]
	v_mov_b64_e32 v[24:25], s[12:13]
	v_mad_i64_i32 v[22:23], s[2:3], v22, s52, v[24:25]
	v_pk_mul_f32 v[24:25], v[16:17], v[36:37]
	v_pk_mul_f32 v[26:27], v[14:15], v[34:35]
	v_pk_mul_f32 v[14:15], v[14:15], v[34:35] op_sel:[1,0] op_sel_hi:[0,1]
	v_pk_mul_f32 v[16:17], v[16:17], v[36:37] op_sel:[1,0] op_sel_hi:[0,1]
	v_add_f32_e32 v14, v14, v15
	v_sub_f32_e32 v15, v24, v25
	v_add_f32_e32 v16, v16, v17
	v_sub_f32_e32 v26, v26, v27
	v_cvt_pk_bf16_f32 v14, v26, v14
	v_cvt_pk_bf16_f32 v15, v15, v16
	v_pk_mul_f32 v[16:17], v[10:11], v[18:19]
	v_pk_mul_f32 v[10:11], v[10:11], v[18:19] op_sel:[1,0] op_sel_hi:[0,1]
	v_sub_f32_e32 v16, v16, v17
	v_add_f32_e32 v10, v10, v11
	v_pk_mul_f32 v[24:25], v[12:13], v[20:21]
	v_cvt_pk_bf16_f32 v16, v16, v10
	v_pk_mul_f32 v[10:11], v[12:13], v[20:21] op_sel:[1,0] op_sel_hi:[0,1]
	v_sub_f32_e32 v17, v24, v25
	v_add_f32_e32 v10, v10, v11
	v_cvt_pk_bf16_f32 v17, v17, v10
	v_pk_mul_f32 v[10:11], v[8:9], v[36:37]
	v_pk_mul_f32 v[12:13], v[6:7], v[34:35]
	v_pk_mul_f32 v[6:7], v[6:7], v[34:35] op_sel:[1,0] op_sel_hi:[0,1]
	v_pk_mul_f32 v[8:9], v[8:9], v[36:37] op_sel:[1,0] op_sel_hi:[0,1]
	v_lshl_add_u64 v[22:23], v[154:155], 1, v[22:23]
	v_add_f32_e32 v6, v6, v7
	v_sub_f32_e32 v7, v10, v11
	v_add_f32_e32 v8, v8, v9
	global_store_dwordx4 v[22:23], v[14:17], off nt
	v_sub_f32_e32 v12, v12, v13
	v_cvt_pk_bf16_f32 v6, v12, v6
	v_cvt_pk_bf16_f32 v7, v7, v8
	v_pk_mul_f32 v[8:9], v[2:3], v[18:19]
	v_pk_mul_f32 v[2:3], v[2:3], v[18:19] op_sel:[1,0] op_sel_hi:[0,1]
	v_pk_mul_f32 v[10:11], v[4:5], v[20:21]
	v_sub_f32_e32 v8, v8, v9
	v_add_f32_e32 v2, v2, v3
	v_cvt_pk_bf16_f32 v8, v8, v2
	v_sub_f32_e32 v9, v10, v11
	v_pk_mul_f32 v[2:3], v[4:5], v[20:21] op_sel:[1,0] op_sel_hi:[0,1]
	s_andn2_b64 vcc, exec, s[24:25]
	s_mov_b64 s[24:25], -1
	v_add_f32_e32 v2, v2, v3
	v_cvt_pk_bf16_f32 v9, v9, v2
	global_store_dwordx4 v[22:23], v[6:9], off offset:256 nt
	s_cbranch_vccnz .LBB0_2541
	s_andn2_b64 vcc, exec, s[6:7]
	s_cbranch_vccnz .LBB0_2540
	s_barrier
	s_branch .LBB0_2540

	.amdhsa_kernel _Z10fwd_kernelILin1EEv4Args
		.amdhsa_group_segment_fixed_size 0
		.amdhsa_private_segment_fixed_size 0
		.amdhsa_kernarg_size 520
		.amdhsa_user_sgpr_count 2
		.amdhsa_user_sgpr_dispatch_ptr 0
		.amdhsa_user_sgpr_queue_ptr 0
		.amdhsa_user_sgpr_kernarg_segment_ptr 1
		.amdhsa_user_sgpr_dispatch_id 0
		.amdhsa_user_sgpr_kernarg_preload_length 0
		.amdhsa_user_sgpr_kernarg_preload_offset 0
		.amdhsa_user_sgpr_private_segment_size 0
		.amdhsa_uses_dynamic_stack 0
		.amdhsa_enable_private_segment 0
		.amdhsa_system_sgpr_workgroup_id_x 1
		.amdhsa_system_sgpr_workgroup_id_y 0
		.amdhsa_system_sgpr_workgroup_id_z 0
		.amdhsa_system_sgpr_workgroup_info 0
		.amdhsa_system_vgpr_workitem_id 0
		.amdhsa_next_free_vgpr 240
		.amdhsa_next_free_sgpr 98
		.amdhsa_accum_offset 240
		.amdhsa_reserve_vcc 1
		.amdhsa_float_round_mode_32 0
		.amdhsa_float_round_mode_16_64 0
		.amdhsa_float_denorm_mode_32 3
		.amdhsa_float_denorm_mode_16_64 3
		.amdhsa_dx10_clamp 1
		.amdhsa_ieee_mode 1
		.amdhsa_fp16_overflow 0
		.amdhsa_tg_split 0
		.amdhsa_exception_fp_ieee_invalid_op 0
		.amdhsa_exception_fp_denorm_src 0
		.amdhsa_exception_fp_ieee_div_zero 0
		.amdhsa_exception_fp_ieee_overflow 0
		.amdhsa_exception_fp_ieee_underflow 0
		.amdhsa_exception_fp_ieee_inexact 0
		.amdhsa_exception_int_div_zero 0
	.end_amdhsa_kernel

amdhsa.kernels:
  - .agpr_count:     0
    .args:
      - .offset:         0
        .size:           264
        .value_kind:     by_value
      - .offset:         264
        .size:           4
        .value_kind:     hidden_block_count_x
      - .offset:         268
        .size:           4
        .value_kind:     hidden_block_count_y
      - .offset:         272
        .size:           4
        .value_kind:     hidden_block_count_z
      - .offset:         276
        .size:           2
        .value_kind:     hidden_group_size_x
      - .offset:         278
        .size:           2
        .value_kind:     hidden_group_size_y
      - .offset:         280
        .size:           2
        .value_kind:     hidden_group_size_z
      - .offset:         282
        .size:           2
        .value_kind:     hidden_remainder_x
      - .offset:         284
        .size:           2
        .value_kind:     hidden_remainder_y
      - .offset:         286
        .size:           2
        .value_kind:     hidden_remainder_z
      - .offset:         304
        .size:           8
        .value_kind:     hidden_global_offset_x
      - .offset:         312
        .size:           8
        .value_kind:     hidden_global_offset_y
      - .offset:         320
        .size:           8
        .value_kind:     hidden_global_offset_z
      - .offset:         328
        .size:           2
        .value_kind:     hidden_grid_dims
      - .offset:         384
        .size:           4
        .value_kind:     hidden_dynamic_lds_size
    .group_segment_fixed_size: 0
    .kernarg_segment_align: 8
    .kernarg_segment_size: 520
    .language:       OpenCL C
    .language_version:
      - 2
      - 0
    .max_flat_workgroup_size: 512
    .name:           _Z10fwd_kernelILin1EEv4Args
    .private_segment_fixed_size: 0
    .sgpr_count:     104
    .sgpr_spill_count: 135
    .symbol:         _Z10fwd_kernelILin1EEv4Args.kd
    .uniform_work_group_size: 1
    .uses_dynamic_stack: false
    .vgpr_count:     240
    .vgpr_spill_count: 0
    .wavefront_size: 64
